# forward-sweep state update: address of the fragment reads precomputed and the first four fragment pairs requested 35 instructions earlier
# speedup vs baseline: 1.0085x; 1.0085x over previous
; #define LAS __attribute__((address_space(3)))
; __device__ __forceinline__ bf16x8 pack8(const float (&f)[8]) { u32x4 u; u.x = cvtpk(f[0], f[1]); u.y = cvtpk(f[2], f[3]); u.z = cvtpk(f[4], f[5]); u.w = cvtpk(f[6], f[7]); return __builtin_bit_cast(bf16x8, u); }
; __device__ __forceinline__ void kv_store(LAS unsigned char* lds, const KVRaw& R, int tid) {
; #pragma unroll
;     for (int i = 0; i < 2; ++i) {
;         const int q2 = tid + 512 * i, row = q2 >> 3, pc = q2 & 7;
;         float fa[8], fb[8], o1[8], o2[8];
;         unpack8(R.ka[i], fa); unpack8(R.kb[i], fb);
;         const float cs[8] = {R.c0[i].x, R.c0[i].y, R.c0[i].z, R.c0[i].w, R.c1[i].x, R.c1[i].y, R.c1[i].z, R.c1[i].w}, sn[8] = {R.s0[i].x, R.s0[i].y, R.s0[i].z, R.s0[i].w, R.s1[i].x, R.s1[i].y, R.s1[i].z, R.s1[i].w};
; #pragma unroll
;         for (int e = 0; e < 8; ++e) { o1[e] = fa[e] * cs[e] - fb[e] * sn[e]; o2[e] = fb[e] * cs[e] + fa[e] * sn[e]; }
;         *(LAS bf16x8*)(lds + LK + offb(row, pc)) = pack8(o1); *(LAS bf16x8*)(lds + LK + offb(row, pc + 8)) = pack8(o2);
;     }
; #pragma unroll
;     for (int i = 0; i < 4; ++i) { const int q4 = tid + 512 * i, row = q4 >> 4, ch = q4 & 15; *(LAS bf16x8*)(lds + LV + offb(row, ch)) = R.v[i]; }
; }
; __device__ __forceinline__ void unit(const bf16_t* __restrict__ proj, const float* __restrict__ rope, const float* __restrict__ log_decay, const float* __restrict__ gn_g, bf16_t* __restrict__ ymix, ...
;     ...
;     for (int n = 0; n < n0; ++n) {
;         RET_LANE
;         float lf2 = lf2_; asm volatile("" : "+v"(lf2));
;         __syncthreads();
;         kv_store(lds, raw, tid);
;         __syncthreads();
.LBB0_287:
	s_waitcnt vmcnt(15)
	v_lshlrev_b32_e32 v100, 16, v76
	v_and_b32_e32 v101, 0xffff0000, v76
	s_waitcnt vmcnt(14)
	v_lshlrev_b32_e32 v102, 16, v72
	v_and_b32_e32 v103, 0xffff0000, v72
	s_waitcnt vmcnt(10)
	v_pk_mul_f32 v[104:105], v[92:93], v[100:101]
	v_pk_mul_f32 v[92:93], v[92:93], v[102:103]
	v_lshlrev_b32_e32 v76, 16, v77
	v_and_b32_e32 v77, 0xffff0000, v77
	v_pk_fma_f32 v[104:105], v[88:89], v[102:103], v[104:105]
	v_pk_fma_f32 v[88:89], v[88:89], v[100:101], v[92:93] neg_lo:[0,0,1] neg_hi:[0,0,1]
	v_lshlrev_b32_e32 v72, 16, v73
	v_and_b32_e32 v73, 0xffff0000, v73
	v_pk_mul_f32 v[92:93], v[94:95], v[76:77]
	v_mov_b32_e32 v98, v201
	v_pk_fma_f32 v[92:93], v[90:91], v[72:73], v[92:93]
	v_pk_mul_f32 v[72:73], v[94:95], v[72:73]
	v_mov_b32_e32 v115, v203
	v_pk_fma_f32 v[76:77], v[90:91], v[76:77], v[72:73] neg_lo:[0,0,1] neg_hi:[0,0,1]
	v_lshlrev_b32_e32 v72, 16, v78
	v_and_b32_e32 v73, 0xffff0000, v78
	v_lshlrev_b32_e32 v90, 16, v74
	v_and_b32_e32 v91, 0xffff0000, v74
	v_pk_mul_f32 v[94:95], v[84:85], v[72:73]
	v_pk_mul_f32 v[84:85], v[84:85], v[90:91]
	v_pk_fma_f32 v[94:95], v[80:81], v[90:91], v[94:95]
	v_pk_fma_f32 v[80:81], v[80:81], v[72:73], v[84:85] neg_lo:[0,0,1] neg_hi:[0,0,1]
	v_lshlrev_b32_e32 v72, 16, v79
	v_and_b32_e32 v73, 0xffff0000, v79
	v_lshlrev_b32_e32 v97, 4, v98
	v_lshlrev_b32_e32 v74, 16, v75
	v_and_b32_e32 v75, 0xffff0000, v75
	v_pk_mul_f32 v[78:79], v[86:87], v[72:73]
	v_and_b32_e32 v96, 0x70, v97
	v_pk_fma_f32 v[78:79], v[82:83], v[74:75], v[78:79]
	v_pk_mul_f32 v[74:75], v[86:87], v[74:75]
	v_add_u32_e32 v96, 0, v96
	v_pk_fma_f32 v[82:83], v[82:83], v[72:73], v[74:75] neg_lo:[0,0,1] neg_hi:[0,0,1]
	v_ashrrev_i32_e32 v84, 3, v98
	v_cvt_pk_bf16_f32 v72, v88, v89
	v_cvt_pk_bf16_f32 v73, v76, v77
	v_cvt_pk_bf16_f32 v74, v80, v81
	v_cvt_pk_bf16_f32 v75, v82, v83
	v_mad_u64_u32 v[76:77], s[38:39], v84, s68, v[96:97]
	s_barrier
	ds_write_b128 v76, v[72:75]
	v_cvt_pk_bf16_f32 v72, v104, v105
	v_cvt_pk_bf16_f32 v73, v92, v93
	v_cvt_pk_bf16_f32 v74, v94, v95
	v_cvt_pk_bf16_f32 v75, v78, v79
	ds_write_b128 v76, v[72:75] offset:128
	s_waitcnt vmcnt(9)
	v_lshlrev_b32_e32 v72, 16, v44
	v_and_b32_e32 v73, 0xffff0000, v44
	s_waitcnt vmcnt(8)
	v_lshlrev_b32_e32 v74, 16, v40
	v_and_b32_e32 v75, 0xffff0000, v40
	s_waitcnt vmcnt(4)
	v_pk_mul_f32 v[76:77], v[68:69], v[72:73]
	v_pk_mul_f32 v[68:69], v[68:69], v[74:75]
	v_lshlrev_b32_e32 v44, 16, v45
	v_and_b32_e32 v45, 0xffff0000, v45
	v_pk_fma_f32 v[76:77], v[64:65], v[74:75], v[76:77]
	v_pk_fma_f32 v[64:65], v[64:65], v[72:73], v[68:69] neg_lo:[0,0,1] neg_hi:[0,0,1]
	v_lshlrev_b32_e32 v40, 16, v41
	v_and_b32_e32 v41, 0xffff0000, v41
	v_pk_mul_f32 v[68:69], v[70:71], v[44:45]
	v_add_u32_e32 v78, 0x200, v98
	v_pk_fma_f32 v[68:69], v[66:67], v[40:41], v[68:69]
	v_pk_mul_f32 v[40:41], v[70:71], v[40:41]
	v_ashrrev_i32_e32 v99, 4, v78
	v_pk_fma_f32 v[40:41], v[66:67], v[44:45], v[40:41] neg_lo:[0,0,1] neg_hi:[0,0,1]
	v_lshlrev_b32_e32 v44, 16, v46
	v_and_b32_e32 v45, 0xffff0000, v46
	v_lshlrev_b32_e32 v66, 16, v42
	v_and_b32_e32 v67, 0xffff0000, v42
	v_pk_mul_f32 v[70:71], v[36:37], v[44:45]
	v_pk_mul_f32 v[36:37], v[36:37], v[66:67]
	v_pk_fma_f32 v[70:71], v[32:33], v[66:67], v[70:71]
	v_pk_fma_f32 v[36:37], v[32:33], v[44:45], v[36:37] neg_lo:[0,0,1] neg_hi:[0,0,1]
	v_lshlrev_b32_e32 v32, 16, v47
	v_and_b32_e32 v33, 0xffff0000, v47
	v_lshlrev_b32_e32 v42, 16, v43
	v_and_b32_e32 v43, 0xffff0000, v43
	v_pk_mul_f32 v[44:45], v[38:39], v[32:33]
	v_pk_mul_f32 v[38:39], v[38:39], v[42:43]
	v_pk_fma_f32 v[44:45], v[34:35], v[42:43], v[44:45]
	v_pk_fma_f32 v[38:39], v[34:35], v[32:33], v[38:39] neg_lo:[0,0,1] neg_hi:[0,0,1]
	v_ashrrev_i32_e32 v42, 3, v78
	v_cvt_pk_bf16_f32 v32, v64, v65
	v_cvt_pk_bf16_f32 v33, v40, v41
	v_cvt_pk_bf16_f32 v34, v36, v37
	v_cvt_pk_bf16_f32 v35, v38, v39
	v_mad_u64_u32 v[36:37], s[38:39], v42, s68, v[96:97]
	ds_write_b128 v36, v[32:35]
	v_cvt_pk_bf16_f32 v32, v76, v77
	v_cvt_pk_bf16_f32 v33, v68, v69
	v_cvt_pk_bf16_f32 v34, v70, v71
	v_cvt_pk_bf16_f32 v35, v44, v45
	v_and_b32_e32 v96, 0xf0, v97
	ds_write_b128 v36, v[32:35] offset:128
	v_add_u32_e32 v32, 0, v96
	v_ashrrev_i32_e32 v97, 4, v98
	v_mad_u64_u32 v[34:35], s[38:39], v97, s68, v[32:33]
	s_waitcnt vmcnt(2)
	ds_write_b128 v34, v[48:51] offset:36864
	v_mad_u64_u32 v[34:35], s[38:39], v99, s68, v[32:33]
	v_add_u32_e32 v33, 0x400, v98
	v_ashrrev_i32_e32 v100, 4, v33
	s_waitcnt vmcnt(1)
	ds_write_b128 v34, v[52:55] offset:36864
	v_mad_u64_u32 v[34:35], s[38:39], v100, s68, v[32:33]
	v_add_u32_e32 v33, 0x600, v98
	v_ashrrev_i32_e32 v101, 4, v33
	v_mad_u64_u32 v[32:33], s[38:39], v101, s68, v[32:33]
	v_lshlrev_b32_e32 v102, 3, v98
	s_add_i32 s9, s3, s4
	ds_write_b128 v34, v[60:63] offset:36864
	s_waitcnt vmcnt(0)
	ds_write_b128 v32, v[56:59] offset:36864
	v_and_b32_e32 v38, 56, v102
	v_add_u32_e32 v34, s9, v84
	v_mov_b64_e32 v[56:57], s[30:31]
	v_lshlrev_b32_e32 v176, 2, v38
	v_mad_i64_i32 v[34:35], s[38:39], v34, s67, v[56:57]
	v_lshl_add_u64 v[32:33], s[20:21], 0, v[176:177]
	v_lshl_add_u64 v[36:37], s[14:15], 0, v[176:177]
	v_lshl_add_u64 v[34:35], v[34:35], 0, v[180:181]
	v_lshlrev_b32_e32 v176, 1, v38
	v_lshl_add_u64 v[34:35], v[34:35], 0, v[176:177]
	v_lshl_add_u64 v[38:39], v[34:35], 0, s[22:23]
	v_add_co_u32_e32 v34, vcc, s69, v34
	v_add_u32_e32 v40, s4, v84
	s_nop 0
	v_addc_co_u32_e32 v35, vcc, 0, v35, vcc
	s_waitcnt lgkmcnt(0)
	s_barrier
; __device__ __forceinline__ bf16x8 pack8(const float (&f)[8]) { u32x4 u; u.x = cvtpk(f[0], f[1]); u.y = cvtpk(f[2], f[3]); u.z = cvtpk(f[4], f[5]); u.w = cvtpk(f[6], f[7]); return __builtin_bit_cast(bf16x8, u); }
; __device__ __forceinline__ void kv_load(KVRaw& R, const bf16_t* __restrict__ proj, const float* __restrict__ rope, int b, int h, int n, int tid) {
; #pragma unroll
;     for (int i = 0; i < 2; ++i) {
;         const int q2 = tid + 512 * i, row = q2 >> 3, pc = q2 & 7, t = n * 128 + row;
;         const bf16_t* rp = proj + (size_t)(b * SEQ + t) * DIN + OFF_KR + h * 128;
;         R.ka[i] = *(const bf16x8*)(rp + pc * 8); R.kb[i] = *(const bf16x8*)(rp + 64 + pc * 8);
;         R.c0[i] = *(const f32x4*)(rope + t * 64 + pc * 8); R.c1[i] = *(const f32x4*)(rope + t * 64 + pc * 8 + 4);
;         R.s0[i] = *(const f32x4*)(rope + SEQ * 64 + t * 64 + pc * 8); R.s1[i] = *(const f32x4*)(rope + SEQ * 64 + t * 64 + pc * 8 + 4);
;     }
; #pragma unroll
;     for (int i = 0; i < 4; ++i) { const int q4 = tid + 512 * i, row = q4 >> 4, ch = q4 & 15, t = n * 128 + row;
;         R.v[i] = *(const bf16x8*)(proj + (size_t)(b * SEQ + t) * DIN + OFF_VR + h * 128 + ch * 8); }
; template <bool FWD> __device__ __forceinline__ void state_update_1(LAS unsigned char* lds, f32x4 (&racc)[8], float l2, int w, int g, unsigned qp, unsigned p) {
;     const float dec = __builtin_amdgcn_exp2f(128.f * l2);
;     bf16x8 vs[4];
; #pragma unroll
;     for (int ks = 0; ks < 4; ++ks) {
;         float f[8]; unpack8(trfrag(lds + LV, 32 * ks + 4 * g, 32 * ks + 16 + 4 * g, w, qp, p), f);
; #pragma unroll
;         for (int e = 0; e < 8; ++e) { const int key = 32 * ks + 16 * (e >> 2) + 4 * g + (e & 3); f[e] *= __builtin_amdgcn_exp2f((FWD ? (float)(127 - key) : (float)key) * l2); }
;         vs[ks] = pack8(f);
	global_load_dwordx4 v[76:79], v[34:35], off
	global_load_dwordx4 v[72:75], v[38:39], off offset:128
	v_lshl_add_u32 v34, v40, 6, v199
	v_ashrrev_i32_e32 v35, 31, v34
	v_lshlrev_b64 v[34:35], 2, v[34:35]
	v_lshl_add_u64 v[38:39], v[32:33], 0, v[34:35]
	v_lshl_add_u64 v[34:35], v[36:37], 0, v[34:35]
	global_load_dwordx4 v[80:83], v[38:39], off offset:16
	global_load_dwordx4 v[88:91], v[38:39], off
	global_load_dwordx4 v[84:87], v[34:35], off offset:16
	global_load_dwordx4 v[92:95], v[34:35], off
	v_add_u32_e32 v34, s9, v42
	v_mad_i64_i32 v[34:35], s[38:39], v34, s67, v[56:57]
	v_lshl_add_u64 v[34:35], v[34:35], 0, v[180:181]
	v_lshl_add_u64 v[34:35], v[34:35], 0, v[176:177]
	v_lshl_add_u64 v[38:39], v[34:35], 0, s[22:23]
	v_add_co_u32_e32 v34, vcc, s69, v34
	v_add_u32_e32 v48, s4, v42
	s_nop 0
	v_addc_co_u32_e32 v35, vcc, 0, v35, vcc
	global_load_dwordx4 v[44:47], v[34:35], off
	global_load_dwordx4 v[40:43], v[38:39], off offset:128
	v_lshl_add_u32 v34, v48, 6, v199
	v_ashrrev_i32_e32 v35, 31, v34
	v_lshlrev_b64 v[38:39], 2, v[34:35]
	v_lshl_add_u64 v[48:49], v[32:33], 0, v[38:39]
	global_load_dwordx4 v[32:35], v[48:49], off offset:16
	global_load_dwordx4 v[64:67], v[48:49], off
	v_lshl_add_u64 v[48:49], v[36:37], 0, v[38:39]
	global_load_dwordx4 v[36:39], v[48:49], off offset:16
	global_load_dwordx4 v[68:71], v[48:49], off
	v_add_u32_e32 v48, s9, v97
	v_mad_i64_i32 v[48:49], s[38:39], v48, s67, v[56:57]
	v_lshl_add_u64 v[48:49], v[48:49], 0, v[180:181]
	v_mov_b32_e32 v97, v177
	v_add_u32_e32 v52, s9, v99
	v_lshl_add_u64 v[48:49], v[48:49], 0, v[96:97]
	v_mad_i64_i32 v[52:53], s[38:39], v52, s67, v[56:57]
	v_add_co_u32_e32 v48, vcc, s69, v48
	v_lshl_add_u64 v[52:53], v[52:53], 0, v[180:181]
	v_add_u32_e32 v58, s9, v100
	v_addc_co_u32_e32 v49, vcc, 0, v49, vcc
	v_lshl_add_u64 v[52:53], v[52:53], 0, v[96:97]
	v_mad_i64_i32 v[58:59], s[38:39], v58, s67, v[56:57]
	v_add_co_u32_e32 v52, vcc, s69, v52
	v_lshl_add_u64 v[58:59], v[58:59], 0, v[180:181]
	s_nop 0
	v_addc_co_u32_e32 v53, vcc, 0, v53, vcc
	v_lshl_add_u64 v[58:59], v[58:59], 0, v[96:97]
	v_add_co_u32_e32 v58, vcc, s69, v58
	v_and_b32_e32 v118, 16, v102
	s_nop 0
	v_addc_co_u32_e32 v59, vcc, 0, v59, vcc
	global_load_dwordx4 v[60:63], v[58:59], off offset:1024
	v_add_u32_e32 v58, s9, v101
	v_mad_i64_i32 v[56:57], s[38:39], v58, s67, v[56:57]
	v_lshl_add_u64 v[56:57], v[56:57], 0, v[180:181]
	v_lshl_add_u64 v[56:57], v[56:57], 0, v[96:97]
	v_bfe_u32 v97, v98, 2, 4
	v_add_co_u32_e32 v56, vcc, s69, v56
	v_and_b32_e32 v116, 8, v102
	v_add_u32_e32 v96, s77, v118
	v_mul_u32_u24_e32 v117, 0x120, v97
	v_lshrrev_b32_e32 v114, 2, v98
	v_addc_co_u32_e32 v57, vcc, 0, v57, vcc
	v_add3_u32 v120, v96, v116, v117
	s_movk_i32 s9, 0x7e
	global_load_dwordx4 v[48:51], v[48:49], off offset:1024
	v_bitop3_b32 v100, v114, s66, 12 bitop3:0x6c
	global_load_dwordx4 v[52:55], v[52:53], off offset:1024
	v_bitop3_b32 v101, v114, s9, 12 bitop3:0x6c
	global_load_dwordx4 v[56:59], v[56:57], off offset:1024
	ds_read_b64_tr_b16 v[98:99], v120 offset:36864
	ds_read_b64_tr_b16 v[96:97], v120 offset:41472
	v_cvt_f32_ubyte0_e32 v100, v100
	v_cvt_f32_ubyte0_e32 v101, v101
	v_mul_f32_e32 v100, v115, v100
	v_mul_f32_e32 v101, v115, v101
	v_exp_f32_e32 v100, v100
	v_exp_f32_e32 v101, v101
	s_movk_i32 s9, 0x7d
	s_waitcnt lgkmcnt(1)
	v_lshlrev_b32_e32 v102, 16, v98
	v_and_b32_e32 v103, 0xffff0000, v98
	v_bitop3_b32 v98, v114, s9, 12 bitop3:0x6c
	v_cvt_f32_ubyte0_e32 v98, v98
	v_mul_f32_e32 v98, v115, v98
	s_movk_i32 s9, 0x7c
	v_pk_mul_f32 v[100:101], v[100:101], v[102:103]
	v_exp_f32_e32 v102, v98
	v_bitop3_b32 v98, v114, s9, 12 bitop3:0x6c
	v_cvt_f32_ubyte0_e32 v98, v98
	v_mul_f32_e32 v98, v115, v98
	v_exp_f32_e32 v103, v98
	v_lshlrev_b32_e32 v98, 16, v99
	v_and_b32_e32 v99, 0xffff0000, v99
	s_movk_i32 s9, 0x6f
	v_pk_mul_f32 v[98:99], v[102:103], v[98:99]
	v_bitop3_b32 v102, v114, s9, 12 bitop3:0x6c
	s_movk_i32 s9, 0x6e
	v_bitop3_b32 v103, v114, s9, 12 bitop3:0x6c
	v_cvt_f32_ubyte0_e32 v102, v102
	v_cvt_f32_ubyte0_e32 v103, v103
	v_mul_f32_e32 v102, v115, v102
	v_mul_f32_e32 v103, v115, v103
	v_exp_f32_e32 v102, v102
	v_exp_f32_e32 v103, v103
	s_movk_i32 s9, 0x6d
	s_waitcnt lgkmcnt(0)
	v_lshlrev_b32_e32 v104, 16, v96
	v_and_b32_e32 v105, 0xffff0000, v96
	v_bitop3_b32 v96, v114, s9, 12 bitop3:0x6c
	v_cvt_f32_ubyte0_e32 v96, v96
	v_mul_f32_e32 v96, v115, v96
	s_movk_i32 s9, 0x6c
	v_pk_mul_f32 v[102:103], v[102:103], v[104:105]
	v_exp_f32_e32 v104, v96
	v_bitop3_b32 v96, v114, s9, 12 bitop3:0x6c
	v_cvt_f32_ubyte0_e32 v96, v96
	v_mul_f32_e32 v96, v115, v96
	v_exp_f32_e32 v105, v96
	v_lshlrev_b32_e32 v96, 16, v97
	v_and_b32_e32 v97, 0xffff0000, v97
	s_movk_i32 s9, 0x5f
	v_pk_mul_f32 v[104:105], v[104:105], v[96:97]
	v_cvt_pk_bf16_f32 v97, v98, v99
	v_cvt_pk_bf16_f32 v98, v102, v103
	v_bitop3_b32 v102, v114, s9, 12 bitop3:0x6c
	s_movk_i32 s9, 0x5e
	v_cvt_pk_bf16_f32 v96, v100, v101
	v_cvt_pk_bf16_f32 v99, v104, v105
	ds_read_b64_tr_b16 v[104:105], v120 offset:46080
	ds_read_b64_tr_b16 v[100:101], v120 offset:50688
	v_bitop3_b32 v103, v114, s9, 12 bitop3:0x6c
	v_cvt_f32_ubyte0_e32 v102, v102
	v_cvt_f32_ubyte0_e32 v103, v103
	v_mul_f32_e32 v102, v115, v102
	v_mul_f32_e32 v103, v115, v103
	v_exp_f32_e32 v102, v102
	v_exp_f32_e32 v103, v103
	s_movk_i32 s9, 0x5d
	s_waitcnt lgkmcnt(1)
; __device__ __forceinline__ bf16x8 pack8(const float (&f)[8]) { u32x4 u; u.x = cvtpk(f[0], f[1]); u.y = cvtpk(f[2], f[3]); u.z = cvtpk(f[4], f[5]); u.w = cvtpk(f[6], f[7]); return __builtin_bit_cast(bf16x8, u); }
; template <bool FWD> __device__ __forceinline__ void state_update_1(LAS unsigned char* lds, f32x4 (&racc)[8], float l2, int w, int g, unsigned qp, unsigned p) {
;     const float dec = __builtin_amdgcn_exp2f(128.f * l2);
;     bf16x8 vs[4];
; #pragma unroll
;     for (int ks = 0; ks < 4; ++ks) {
;         float f[8]; unpack8(trfrag(lds + LV, 32 * ks + 4 * g, 32 * ks + 16 + 4 * g, w, qp, p), f);
; #pragma unroll
;         for (int e = 0; e < 8; ++e) { const int key = 32 * ks + 16 * (e >> 2) + 4 * g + (e & 3); f[e] *= __builtin_amdgcn_exp2f((FWD ? (float)(127 - key) : (float)key) * l2); }
;         vs[ks] = pack8(f);
;     }
; #pragma unroll
;     for (int nb = 0; nb < 8; ++nb) {
;         racc[nb] = racc[nb] * dec;
; #pragma unroll
;         for (int ks = 0; ks < 4; ++ks) racc[nb] = __builtin_amdgcn_mfma_f32_16x16x32_bf16(vs[ks], trfrag(lds + LK, 32 * ks + 4 * g, 32 * ks + 16 + 4 * g, nb, qp, p), racc[nb], 0, 0, 0);
;     }
	v_lshlrev_b32_e32 v106, 16, v104
	v_and_b32_e32 v107, 0xffff0000, v104
	v_bitop3_b32 v104, v114, s9, 12 bitop3:0x6c
	v_cvt_f32_ubyte0_e32 v104, v104
	v_mul_f32_e32 v104, v115, v104
	s_movk_i32 s9, 0x5c
	v_pk_mul_f32 v[102:103], v[102:103], v[106:107]
	v_exp_f32_e32 v106, v104
	v_bitop3_b32 v104, v114, s9, 12 bitop3:0x6c
	v_cvt_f32_ubyte0_e32 v104, v104
	v_mul_f32_e32 v104, v115, v104
	v_exp_f32_e32 v107, v104
	v_lshlrev_b32_e32 v104, 16, v105
	v_and_b32_e32 v105, 0xffff0000, v105
	s_movk_i32 s9, 0x4f
	v_pk_mul_f32 v[106:107], v[106:107], v[104:105]
	v_bitop3_b32 v104, v114, s9, 12 bitop3:0x6c
	s_movk_i32 s9, 0x4e
	v_bitop3_b32 v105, v114, s9, 12 bitop3:0x6c
	v_cvt_f32_ubyte0_e32 v104, v104
	v_cvt_f32_ubyte0_e32 v105, v105
	v_mul_f32_e32 v104, v115, v104
	v_mul_f32_e32 v105, v115, v105
	v_exp_f32_e32 v104, v104
	v_exp_f32_e32 v105, v105
	s_movk_i32 s9, 0x4d
	s_waitcnt lgkmcnt(0)
	v_lshlrev_b32_e32 v108, 16, v100
	v_and_b32_e32 v109, 0xffff0000, v100
	v_bitop3_b32 v100, v114, s9, 12 bitop3:0x6c
	v_cvt_f32_ubyte0_e32 v100, v100
	v_mul_f32_e32 v100, v115, v100
	s_movk_i32 s9, 0x4c
	v_pk_mul_f32 v[108:109], v[104:105], v[108:109]
	v_exp_f32_e32 v104, v100
	v_bitop3_b32 v100, v114, s9, 12 bitop3:0x6c
	v_cvt_f32_ubyte0_e32 v100, v100
	v_mul_f32_e32 v100, v115, v100
	v_exp_f32_e32 v105, v100
	v_lshlrev_b32_e32 v100, 16, v101
	v_and_b32_e32 v101, 0xffff0000, v101
	v_bitop3_b32 v121, v114, 30, 12 bitop3:0x6c
	v_pk_mul_f32 v[100:101], v[104:105], v[100:101]
	v_cvt_pk_bf16_f32 v104, v102, v103
	v_cvt_pk_bf16_f32 v105, v106, v107
	v_cvt_pk_bf16_f32 v106, v108, v109
	v_cvt_pk_bf16_f32 v107, v100, v101
	ds_read_b64_tr_b16 v[100:101], v120 offset:55296
	ds_read_b64_tr_b16 v[102:103], v120 offset:59904
	v_bitop3_b32 v108, v114, 63, 12 bitop3:0x6c
	v_bitop3_b32 v109, v114, 62, 12 bitop3:0x6c
	v_cvt_f32_ubyte0_e32 v108, v108
	v_cvt_f32_ubyte0_e32 v109, v109
	v_mul_f32_e32 v108, v115, v108
	v_mul_f32_e32 v109, v115, v109
	v_exp_f32_e32 v108, v108
	v_exp_f32_e32 v109, v109
	s_waitcnt lgkmcnt(1)
	v_lshlrev_b32_e32 v110, 16, v100
	v_and_b32_e32 v111, 0xffff0000, v100
	v_bitop3_b32 v100, v114, 61, 12 bitop3:0x6c
	v_cvt_f32_ubyte0_e32 v100, v100
	v_mul_f32_e32 v100, v115, v100
	v_pk_mul_f32 v[108:109], v[108:109], v[110:111]
	v_exp_f32_e32 v110, v100
	v_bitop3_b32 v100, v114, 60, 12 bitop3:0x6c
	v_cvt_f32_ubyte0_e32 v100, v100
	v_mul_f32_e32 v100, v115, v100
	v_exp_f32_e32 v111, v100
	v_lshlrev_b32_e32 v100, 16, v101
	v_and_b32_e32 v101, 0xffff0000, v101
	s_waitcnt lgkmcnt(0)
	v_lshlrev_b32_e32 v122, 16, v102
	v_pk_mul_f32 v[100:101], v[110:111], v[100:101]
	v_bitop3_b32 v110, v114, 47, 12 bitop3:0x6c
	v_bitop3_b32 v111, v114, 46, 12 bitop3:0x6c
	v_cvt_f32_ubyte0_e32 v110, v110
	v_cvt_f32_ubyte0_e32 v111, v111
	v_mul_f32_e32 v110, v115, v110
	v_mul_f32_e32 v111, v115, v111
	v_exp_f32_e32 v110, v110
	v_exp_f32_e32 v111, v111
	v_and_b32_e32 v123, 0xffff0000, v102
	v_bitop3_b32 v102, v114, 45, 12 bitop3:0x6c
	v_cvt_f32_ubyte0_e32 v102, v102
	v_mul_f32_e32 v102, v115, v102
	v_pk_mul_f32 v[110:111], v[110:111], v[122:123]
	v_exp_f32_e32 v122, v102
	v_bitop3_b32 v102, v114, 44, 12 bitop3:0x6c
	v_cvt_f32_ubyte0_e32 v102, v102
	v_mul_f32_e32 v102, v115, v102
	v_exp_f32_e32 v123, v102
	v_lshlrev_b32_e32 v102, 16, v103
	v_and_b32_e32 v103, 0xffff0000, v103
	v_cvt_pk_bf16_f32 v110, v110, v111
	v_pk_mul_f32 v[102:103], v[122:123], v[102:103]
	v_cvt_pk_bf16_f32 v108, v108, v109
	v_cvt_pk_bf16_f32 v111, v102, v103
	v_add_u32_e32 v102, 0xfc00, v120
	v_cvt_pk_bf16_f32 v109, v100, v101
	ds_read_b64_tr_b16 v[100:101], v120 offset:64512
	ds_read_b64_tr_b16 v[102:103], v102 offset:4608
	v_bitop3_b32 v120, v114, 31, 12 bitop3:0x6c
	v_cvt_f32_ubyte0_e32 v120, v120
	v_cvt_f32_ubyte0_e32 v121, v121
	v_mul_f32_e32 v120, v115, v120
	v_mul_f32_e32 v121, v115, v121
	v_exp_f32_e32 v120, v120
	v_exp_f32_e32 v121, v121
	s_waitcnt lgkmcnt(1)
	v_lshlrev_b32_e32 v122, 16, v100
	v_and_b32_e32 v123, 0xffff0000, v100
	v_bitop3_b32 v100, v114, 29, 12 bitop3:0x6c
	v_cvt_f32_ubyte0_e32 v100, v100
	v_mul_f32_e32 v100, v115, v100
	v_pk_mul_f32 v[120:121], v[120:121], v[122:123]
	v_exp_f32_e32 v122, v100
	v_bitop3_b32 v100, v114, 28, 12 bitop3:0x6c
	v_cvt_f32_ubyte0_e32 v100, v100
	v_mul_f32_e32 v100, v115, v100
	v_exp_f32_e32 v123, v100
	v_lshlrev_b32_e32 v100, 16, v101
	v_and_b32_e32 v101, 0xffff0000, v101
	s_waitcnt lgkmcnt(0)
	v_add3_u32 v230, v118, v116, v117
	ds_read_b64_tr_b16 v[222:223], v230
	ds_read_b64_tr_b16 v[224:225], v230 offset:4608
	ds_read_b64_tr_b16 v[226:227], v230 offset:9216
	ds_read_b64_tr_b16 v[228:229], v230 offset:13824
	ds_read_b64_tr_b16 v[236:237], v230 offset:18432
	ds_read_b64_tr_b16 v[238:239], v230 offset:23040
	ds_read_b64_tr_b16 v[240:241], v230 offset:27648
	ds_read_b64_tr_b16 v[242:243], v230 offset:32256
	v_lshlrev_b32_e32 v124, 16, v102
	v_pk_mul_f32 v[122:123], v[122:123], v[100:101]
	v_bitop3_b32 v100, v114, 15, 12 bitop3:0x6c
	v_bitop3_b32 v101, v114, 14, 12 bitop3:0x6c
	v_cvt_f32_ubyte0_e32 v100, v100
	v_cvt_f32_ubyte0_e32 v101, v101
	v_mul_f32_e32 v100, v115, v100
	v_mul_f32_e32 v101, v115, v101
	v_exp_f32_e32 v100, v100
	v_exp_f32_e32 v101, v101
	v_and_b32_e32 v125, 0xffff0000, v102
	v_lshlrev_b32_e32 v102, 16, v103
	v_and_b32_e32 v103, 0xffff0000, v103
	v_pk_mul_f32 v[124:125], v[100:101], v[124:125]
	v_bitop3_b32 v100, v114, 13, 12 bitop3:0x6c
	v_bitop3_b32 v101, v114, 12, v114 bitop3:0xc
	v_cvt_f32_ubyte0_e32 v100, v100
	v_cvt_f32_ubyte0_e32 v101, v101
	v_mul_f32_e32 v100, v115, v100
	v_mul_f32_e32 v101, v115, v101
	v_exp_f32_e32 v100, v100
	v_exp_f32_e32 v101, v101
	v_mul_f32_e32 v119, 0x43000000, v115
	s_addk_i32 s4, 0x80
	s_cmp_eq_u32 s8, s4
	v_pk_mul_f32 v[114:115], v[100:101], v[102:103]
	v_cvt_pk_bf16_f32 v100, v120, v121
	v_cvt_pk_bf16_f32 v103, v114, v115
	v_exp_f32_e32 v114, v119
	v_add_u32_e32 v115, 0, v118
	v_cvt_pk_bf16_f32 v101, v122, v123
	v_cvt_pk_bf16_f32 v102, v124, v125
	v_pk_mul_f32 v[22:23], v[22:23], v[114:115] op_sel_hi:[1,0]
	v_pk_mul_f32 v[20:21], v[20:21], v[114:115] op_sel_hi:[1,0]
	v_add3_u32 v115, v115, v116, v117
	s_waitcnt lgkmcnt(6)
; template <bool FWD> __device__ __forceinline__ void state_update_1(LAS unsigned char* lds, f32x4 (&racc)[8], float l2, int w, int g, unsigned qp, unsigned p) {
;     ...
; #pragma unroll
;     for (int nb = 0; nb < 8; ++nb) {
;         racc[nb] = racc[nb] * dec;
; #pragma unroll
;         for (int ks = 0; ks < 4; ++ks) racc[nb] = __builtin_amdgcn_mfma_f32_16x16x32_bf16(vs[ks], trfrag(lds + LK, 32 * ks + 4 * g, 32 * ks + 16 + 4 * g, nb, qp, p), racc[nb], 0, 0, 0);
;     }
; __device__ __forceinline__ void unit(const bf16_t* __restrict__ proj, const float* __restrict__ rope, const float* __restrict__ log_decay, const float* __restrict__ gn_g, bf16_t* __restrict__ ymix, ...
;     ...
;     for (int n = 0; n < n0; ++n) {
;         RET_LANE
;         float lf2 = lf2_; asm volatile("" : "+v"(lf2));
;         __syncthreads();
;         kv_store(lds, raw, tid);
;         __syncthreads();
;         kv_load(raw, proj, rope, b, h, n + 1, tid);
;         state_update<true>(lds, racc, lf2, w, g, qp, p);
	v_mfma_f32_16x16x32_bf16 v[20:23], v[96:99], v[222:225], v[20:23]
	v_pk_mul_f32 v[2:3], v[2:3], v[114:115] op_sel_hi:[1,0]
	v_pk_mul_f32 v[0:1], v[0:1], v[114:115] op_sel_hi:[1,0]
	ds_read_b64_tr_b16 v[222:223], v115 offset:32
	ds_read_b64_tr_b16 v[224:225], v115 offset:4640
	s_waitcnt lgkmcnt(6)
	v_mfma_f32_16x16x32_bf16 v[20:23], v[104:107], v[226:229], v[20:23]
	v_pk_mul_f32 v[18:19], v[18:19], v[114:115] op_sel_hi:[1,0]
	v_pk_mul_f32 v[16:17], v[16:17], v[114:115] op_sel_hi:[1,0]
	ds_read_b64_tr_b16 v[226:227], v115 offset:9248
	ds_read_b64_tr_b16 v[228:229], v115 offset:13856
	s_waitcnt lgkmcnt(6)
	v_mfma_f32_16x16x32_bf16 v[20:23], v[108:111], v[236:239], v[20:23]
	v_pk_mul_f32 v[26:27], v[26:27], v[114:115] op_sel_hi:[1,0]
	ds_read_b64_tr_b16 v[236:237], v115 offset:18464
	ds_read_b64_tr_b16 v[238:239], v115 offset:23072
	s_waitcnt lgkmcnt(6)
	v_mfma_f32_16x16x32_bf16 v[20:23], v[100:103], v[240:243], v[20:23]
	v_pk_mul_f32 v[24:25], v[24:25], v[114:115] op_sel_hi:[1,0]
	v_pk_mul_f32 v[6:7], v[6:7], v[114:115] op_sel_hi:[1,0]
	ds_read_b64_tr_b16 v[240:241], v115 offset:27680
	ds_read_b64_tr_b16 v[242:243], v115 offset:32288
	s_waitcnt lgkmcnt(6)
	v_mfma_f32_16x16x32_bf16 v[0:3], v[96:99], v[222:225], v[0:3]
	v_mul_f32_e64 v4, v4, v114
	v_mul_f32_e64 v5, v5, v114
	v_pk_mul_f32 v[10:11], v[10:11], v[114:115] op_sel_hi:[1,0]
	v_pk_mul_f32 v[8:9], v[8:9], v[114:115] op_sel_hi:[1,0]
	ds_read_b64_tr_b16 v[222:223], v115 offset:64
	ds_read_b64_tr_b16 v[224:225], v115 offset:4672
	s_waitcnt lgkmcnt(6)
	v_mfma_f32_16x16x32_bf16 v[0:3], v[104:107], v[226:229], v[0:3]
	v_pk_mul_f32 v[14:15], v[14:15], v[114:115] op_sel_hi:[1,0]
	v_pk_mul_f32 v[12:13], v[12:13], v[114:115] op_sel_hi:[1,0]
	ds_read_b64_tr_b16 v[226:227], v115 offset:9280
	ds_read_b64_tr_b16 v[228:229], v115 offset:13888
	s_waitcnt lgkmcnt(6)
	v_mfma_f32_16x16x32_bf16 v[0:3], v[108:111], v[236:239], v[0:3]
	v_pk_mul_f32 v[30:31], v[30:31], v[114:115] op_sel_hi:[1,0]
	v_pk_mul_f32 v[28:29], v[28:29], v[114:115] op_sel_hi:[1,0]
	ds_read_b64_tr_b16 v[236:237], v115 offset:18496
	ds_read_b64_tr_b16 v[238:239], v115 offset:23104
	s_waitcnt lgkmcnt(6)
	v_mfma_f32_16x16x32_bf16 v[0:3], v[100:103], v[240:243], v[0:3]
	ds_read_b64_tr_b16 v[240:241], v115 offset:27712
	ds_read_b64_tr_b16 v[242:243], v115 offset:32320
	s_waitcnt lgkmcnt(6)
	v_mfma_f32_16x16x32_bf16 v[16:19], v[96:99], v[222:225], v[16:19]
	ds_read_b64_tr_b16 v[222:223], v115 offset:96
	ds_read_b64_tr_b16 v[224:225], v115 offset:4704
	s_waitcnt lgkmcnt(6)
	v_mfma_f32_16x16x32_bf16 v[16:19], v[104:107], v[226:229], v[16:19]
	ds_read_b64_tr_b16 v[226:227], v115 offset:9312
	ds_read_b64_tr_b16 v[228:229], v115 offset:13920
	s_waitcnt lgkmcnt(6)
	v_mfma_f32_16x16x32_bf16 v[16:19], v[108:111], v[236:239], v[16:19]
	ds_read_b64_tr_b16 v[236:237], v115 offset:18528
	ds_read_b64_tr_b16 v[238:239], v115 offset:23136
	s_waitcnt lgkmcnt(6)
	v_mfma_f32_16x16x32_bf16 v[16:19], v[100:103], v[240:243], v[16:19]
	ds_read_b64_tr_b16 v[240:241], v115 offset:27744
	ds_read_b64_tr_b16 v[242:243], v115 offset:32352
	s_waitcnt lgkmcnt(6)
	v_mfma_f32_16x16x32_bf16 v[24:27], v[96:99], v[222:225], v[24:27]
	ds_read_b64_tr_b16 v[222:223], v115 offset:128
	ds_read_b64_tr_b16 v[224:225], v115 offset:4736
	s_waitcnt lgkmcnt(6)
	v_mfma_f32_16x16x32_bf16 v[24:27], v[104:107], v[226:229], v[24:27]
	ds_read_b64_tr_b16 v[226:227], v115 offset:9344
	ds_read_b64_tr_b16 v[228:229], v115 offset:13952
	s_waitcnt lgkmcnt(6)
	v_mfma_f32_16x16x32_bf16 v[24:27], v[108:111], v[236:239], v[24:27]
	ds_read_b64_tr_b16 v[236:237], v115 offset:18560
	ds_read_b64_tr_b16 v[238:239], v115 offset:23168
	s_waitcnt lgkmcnt(6)
	v_mfma_f32_16x16x32_bf16 v[24:27], v[100:103], v[240:243], v[24:27]
	ds_read_b64_tr_b16 v[240:241], v115 offset:27776
	ds_read_b64_tr_b16 v[242:243], v115 offset:32384
	s_waitcnt lgkmcnt(6)
	v_mfma_f32_16x16x32_bf16 v[4:7], v[96:99], v[222:225], v[4:7]
	ds_read_b64_tr_b16 v[222:223], v115 offset:160
	ds_read_b64_tr_b16 v[224:225], v115 offset:4768
	s_waitcnt lgkmcnt(6)
	v_mfma_f32_16x16x32_bf16 v[4:7], v[104:107], v[226:229], v[4:7]
	ds_read_b64_tr_b16 v[226:227], v115 offset:9376
	ds_read_b64_tr_b16 v[228:229], v115 offset:13984
	s_waitcnt lgkmcnt(6)
	v_mfma_f32_16x16x32_bf16 v[4:7], v[108:111], v[236:239], v[4:7]
	ds_read_b64_tr_b16 v[236:237], v115 offset:18592
	ds_read_b64_tr_b16 v[238:239], v115 offset:23200
	s_waitcnt lgkmcnt(6)
	v_mfma_f32_16x16x32_bf16 v[4:7], v[100:103], v[240:243], v[4:7]
	ds_read_b64_tr_b16 v[240:241], v115 offset:27808
	ds_read_b64_tr_b16 v[242:243], v115 offset:32416
	s_waitcnt lgkmcnt(6)
	v_mfma_f32_16x16x32_bf16 v[8:11], v[96:99], v[222:225], v[8:11]
	ds_read_b64_tr_b16 v[222:223], v115 offset:192
	ds_read_b64_tr_b16 v[224:225], v115 offset:4800
	s_waitcnt lgkmcnt(6)
	v_mfma_f32_16x16x32_bf16 v[8:11], v[104:107], v[226:229], v[8:11]
	ds_read_b64_tr_b16 v[226:227], v115 offset:9408
	ds_read_b64_tr_b16 v[228:229], v115 offset:14016
	s_waitcnt lgkmcnt(6)
	v_mfma_f32_16x16x32_bf16 v[8:11], v[108:111], v[236:239], v[8:11]
	ds_read_b64_tr_b16 v[236:237], v115 offset:18624
	ds_read_b64_tr_b16 v[238:239], v115 offset:23232
	s_waitcnt lgkmcnt(6)
	v_mfma_f32_16x16x32_bf16 v[8:11], v[100:103], v[240:243], v[8:11]
	ds_read_b64_tr_b16 v[240:241], v115 offset:27840
	ds_read_b64_tr_b16 v[242:243], v115 offset:32448
	s_waitcnt lgkmcnt(6)
	v_mfma_f32_16x16x32_bf16 v[12:15], v[96:99], v[222:225], v[12:15]
	ds_read_b64_tr_b16 v[222:223], v115 offset:224
	ds_read_b64_tr_b16 v[224:225], v115 offset:4832
	s_waitcnt lgkmcnt(6)
	v_mfma_f32_16x16x32_bf16 v[12:15], v[104:107], v[226:229], v[12:15]
	ds_read_b64_tr_b16 v[226:227], v115 offset:9440
	ds_read_b64_tr_b16 v[228:229], v115 offset:14048
	s_waitcnt lgkmcnt(6)
	v_mfma_f32_16x16x32_bf16 v[12:15], v[108:111], v[236:239], v[12:15]
	ds_read_b64_tr_b16 v[236:237], v115 offset:18656
	ds_read_b64_tr_b16 v[238:239], v115 offset:23264
	s_waitcnt lgkmcnt(6)
	v_mfma_f32_16x16x32_bf16 v[12:15], v[100:103], v[240:243], v[12:15]
	ds_read_b64_tr_b16 v[240:241], v115 offset:27872
	ds_read_b64_tr_b16 v[242:243], v115 offset:32480
	s_waitcnt lgkmcnt(6)
	v_mfma_f32_16x16x32_bf16 v[28:31], v[96:99], v[222:225], v[28:31]
	s_waitcnt lgkmcnt(4)
	v_mfma_f32_16x16x32_bf16 v[28:31], v[104:107], v[226:229], v[28:31]
	s_waitcnt lgkmcnt(2)
	v_mfma_f32_16x16x32_bf16 v[28:31], v[108:111], v[236:239], v[28:31]
	s_waitcnt lgkmcnt(0)
	v_mfma_f32_16x16x32_bf16 v[28:31], v[100:103], v[240:243], v[28:31]
	s_cbranch_scc0 .LBB0_287
	s_branch .LBB0_289
